# router weight staging: sixteen loads in flight instead of one load per round trip
# baseline (speedup 1.0000x reference)
; __device__ __forceinline__ void router_ph(const int WID_, const bf16* __restrict__ x3, const float* __restrict__ nw, const float* __restrict__ wrg, const float* __restrict__ brg, ...
;     ...
;     for (int i = wv * 64 + lane; i < 4 * 1024 * 2; i += NT) { const float4 w = *(const float4*)(wre + i * 4);
;         typedef _Float16 h4 __attribute__((ext_vector_type(4))); *(h4*)(we16 + i * 4) = (h4){(_Float16)w.x, (_Float16)w.y, (_Float16)w.z, (_Float16)w.w}; }
.LBB0_2140:
	v_ashrrev_i32_e32 v1, 31, v0
	v_lshl_add_u64 v[114:115], v[0:1], 2, s[14:15]
	global_load_dwordx4 v[132:135], v[114:115], off
	s_mov_b64 s[100:101], 0x2000
	v_lshl_add_u64 v[112:113], v[114:115], 0, s[100:101]
	global_load_dwordx4 v[136:139], v[112:113], off
	s_mov_b64 s[100:101], 0x4000
	v_lshl_add_u64 v[112:113], v[114:115], 0, s[100:101]
	global_load_dwordx4 v[140:143], v[112:113], off
	s_mov_b64 s[100:101], 0x6000
	v_lshl_add_u64 v[112:113], v[114:115], 0, s[100:101]
	global_load_dwordx4 v[144:147], v[112:113], off
	s_mov_b64 s[100:101], 0x8000
	v_lshl_add_u64 v[112:113], v[114:115], 0, s[100:101]
	global_load_dwordx4 v[148:151], v[112:113], off
	s_mov_b64 s[100:101], 0xa000
	v_lshl_add_u64 v[112:113], v[114:115], 0, s[100:101]
	global_load_dwordx4 v[152:155], v[112:113], off
	s_mov_b64 s[100:101], 0xc000
	v_lshl_add_u64 v[112:113], v[114:115], 0, s[100:101]
	global_load_dwordx4 v[156:159], v[112:113], off
	s_mov_b64 s[100:101], 0xe000
	v_lshl_add_u64 v[112:113], v[114:115], 0, s[100:101]
	global_load_dwordx4 v[160:163], v[112:113], off
	s_mov_b64 s[100:101], 0x10000
	v_lshl_add_u64 v[112:113], v[114:115], 0, s[100:101]
	global_load_dwordx4 v[164:167], v[112:113], off
	s_mov_b64 s[100:101], 0x12000
	v_lshl_add_u64 v[112:113], v[114:115], 0, s[100:101]
	global_load_dwordx4 v[168:171], v[112:113], off
	s_mov_b64 s[100:101], 0x14000
	v_lshl_add_u64 v[112:113], v[114:115], 0, s[100:101]
	global_load_dwordx4 v[172:175], v[112:113], off
	s_mov_b64 s[100:101], 0x16000
	v_lshl_add_u64 v[112:113], v[114:115], 0, s[100:101]
	global_load_dwordx4 v[176:179], v[112:113], off
	s_mov_b64 s[100:101], 0x18000
	v_lshl_add_u64 v[112:113], v[114:115], 0, s[100:101]
	global_load_dwordx4 v[180:183], v[112:113], off
	s_mov_b64 s[100:101], 0x1a000
	v_lshl_add_u64 v[112:113], v[114:115], 0, s[100:101]
	global_load_dwordx4 v[184:187], v[112:113], off
	s_mov_b64 s[100:101], 0x1c000
	v_lshl_add_u64 v[112:113], v[114:115], 0, s[100:101]
	global_load_dwordx4 v[188:191], v[112:113], off
	s_mov_b64 s[100:101], 0x1e000
	v_lshl_add_u64 v[112:113], v[114:115], 0, s[100:101]
	global_load_dwordx4 v[108:111], v[112:113], off
	s_waitcnt vmcnt(15)
	v_cvt_f16_f32_e32 v1, v132
	v_cvt_f16_f32_e32 v3, v135
	v_cvt_pk_f16_f32 v5, v133, v134
	v_pack_b32_f16 v6, v1, v5
	v_alignbit_b32 v7, v3, v5, 16
	ds_write_b64 v2, v[6:7]
	v_add_u32_e32 v2, s98, v2
	s_xor_b32 s98, s98, 0x1c00
	s_waitcnt vmcnt(14)
	v_cvt_f16_f32_e32 v1, v136
	v_cvt_f16_f32_e32 v3, v139
	v_cvt_pk_f16_f32 v5, v137, v138
	v_pack_b32_f16 v6, v1, v5
	v_alignbit_b32 v7, v3, v5, 16
	ds_write_b64 v2, v[6:7]
	v_add_u32_e32 v2, s98, v2
	s_xor_b32 s98, s98, 0x1c00
	s_waitcnt vmcnt(13)
	v_cvt_f16_f32_e32 v1, v140
	v_cvt_f16_f32_e32 v3, v143
	v_cvt_pk_f16_f32 v5, v141, v142
	v_pack_b32_f16 v6, v1, v5
	v_alignbit_b32 v7, v3, v5, 16
	ds_write_b64 v2, v[6:7]
	v_add_u32_e32 v2, s98, v2
	s_xor_b32 s98, s98, 0x1c00
	s_waitcnt vmcnt(12)
	v_cvt_f16_f32_e32 v1, v144
	v_cvt_f16_f32_e32 v3, v147
	v_cvt_pk_f16_f32 v5, v145, v146
	v_pack_b32_f16 v6, v1, v5
	v_alignbit_b32 v7, v3, v5, 16
	ds_write_b64 v2, v[6:7]
	v_add_u32_e32 v2, s98, v2
	s_xor_b32 s98, s98, 0x1c00
	s_waitcnt vmcnt(11)
	v_cvt_f16_f32_e32 v1, v148
	v_cvt_f16_f32_e32 v3, v151
	v_cvt_pk_f16_f32 v5, v149, v150
	v_pack_b32_f16 v6, v1, v5
	v_alignbit_b32 v7, v3, v5, 16
	ds_write_b64 v2, v[6:7]
	v_add_u32_e32 v2, s98, v2
	s_xor_b32 s98, s98, 0x1c00
	s_waitcnt vmcnt(10)
	v_cvt_f16_f32_e32 v1, v152
	v_cvt_f16_f32_e32 v3, v155
	v_cvt_pk_f16_f32 v5, v153, v154
	v_pack_b32_f16 v6, v1, v5
	v_alignbit_b32 v7, v3, v5, 16
	ds_write_b64 v2, v[6:7]
	v_add_u32_e32 v2, s98, v2
	s_xor_b32 s98, s98, 0x1c00
	s_waitcnt vmcnt(9)
	v_cvt_f16_f32_e32 v1, v156
	v_cvt_f16_f32_e32 v3, v159
	v_cvt_pk_f16_f32 v5, v157, v158
	v_pack_b32_f16 v6, v1, v5
	v_alignbit_b32 v7, v3, v5, 16
	ds_write_b64 v2, v[6:7]
	v_add_u32_e32 v2, s98, v2
	s_xor_b32 s98, s98, 0x1c00
	s_waitcnt vmcnt(8)
	v_cvt_f16_f32_e32 v1, v160
	v_cvt_f16_f32_e32 v3, v163
	v_cvt_pk_f16_f32 v5, v161, v162
	v_pack_b32_f16 v6, v1, v5
	v_alignbit_b32 v7, v3, v5, 16
	ds_write_b64 v2, v[6:7]
	v_add_u32_e32 v2, s98, v2
	s_xor_b32 s98, s98, 0x1c00
	s_waitcnt vmcnt(7)
	v_cvt_f16_f32_e32 v1, v164
	v_cvt_f16_f32_e32 v3, v167
	v_cvt_pk_f16_f32 v5, v165, v166
	v_pack_b32_f16 v6, v1, v5
	v_alignbit_b32 v7, v3, v5, 16
	ds_write_b64 v2, v[6:7]
	v_add_u32_e32 v2, s98, v2
	s_xor_b32 s98, s98, 0x1c00
	s_waitcnt vmcnt(6)
	v_cvt_f16_f32_e32 v1, v168
	v_cvt_f16_f32_e32 v3, v171
	v_cvt_pk_f16_f32 v5, v169, v170
	v_pack_b32_f16 v6, v1, v5
	v_alignbit_b32 v7, v3, v5, 16
	ds_write_b64 v2, v[6:7]
	v_add_u32_e32 v2, s98, v2
	s_xor_b32 s98, s98, 0x1c00
	s_waitcnt vmcnt(5)
	v_cvt_f16_f32_e32 v1, v172
	v_cvt_f16_f32_e32 v3, v175
	v_cvt_pk_f16_f32 v5, v173, v174
	v_pack_b32_f16 v6, v1, v5
	v_alignbit_b32 v7, v3, v5, 16
	ds_write_b64 v2, v[6:7]
	v_add_u32_e32 v2, s98, v2
	s_xor_b32 s98, s98, 0x1c00
	s_waitcnt vmcnt(4)
	v_cvt_f16_f32_e32 v1, v176
	v_cvt_f16_f32_e32 v3, v179
	v_cvt_pk_f16_f32 v5, v177, v178
	v_pack_b32_f16 v6, v1, v5
	v_alignbit_b32 v7, v3, v5, 16
	ds_write_b64 v2, v[6:7]
	v_add_u32_e32 v2, s98, v2
	s_xor_b32 s98, s98, 0x1c00
	s_waitcnt vmcnt(3)
	v_cvt_f16_f32_e32 v1, v180
	v_cvt_f16_f32_e32 v3, v183
	v_cvt_pk_f16_f32 v5, v181, v182
	v_pack_b32_f16 v6, v1, v5
	v_alignbit_b32 v7, v3, v5, 16
	ds_write_b64 v2, v[6:7]
	v_add_u32_e32 v2, s98, v2
	s_xor_b32 s98, s98, 0x1c00
	s_waitcnt vmcnt(2)
	v_cvt_f16_f32_e32 v1, v184
	v_cvt_f16_f32_e32 v3, v187
	v_cvt_pk_f16_f32 v5, v185, v186
	v_pack_b32_f16 v6, v1, v5
	v_alignbit_b32 v7, v3, v5, 16
	ds_write_b64 v2, v[6:7]
	v_add_u32_e32 v2, s98, v2
	s_xor_b32 s98, s98, 0x1c00
	s_waitcnt vmcnt(1)
	v_cvt_f16_f32_e32 v1, v188
	v_cvt_f16_f32_e32 v3, v191
	v_cvt_pk_f16_f32 v5, v189, v190
	v_pack_b32_f16 v6, v1, v5
	v_alignbit_b32 v7, v3, v5, 16
	ds_write_b64 v2, v[6:7]
	v_add_u32_e32 v2, s98, v2
	s_xor_b32 s98, s98, 0x1c00
	s_waitcnt vmcnt(0)
	v_cvt_f16_f32_e32 v1, v108
	v_cvt_f16_f32_e32 v3, v111
	v_cvt_pk_f16_f32 v5, v109, v110
	v_pack_b32_f16 v6, v1, v5
	v_alignbit_b32 v7, v3, v5, 16
	ds_write_b64 v2, v[6:7]
	v_add_u32_e32 v2, s98, v2
	s_xor_b32 s98, s98, 0x1c00
	s_or_b64 exec, exec, s[4:5]
